# speedup vs baseline: 1.0073x; 1.0058x over previous
_Z9k_binsortPKjPKiPKfPKDv4_jPiS8_PfP6__half:
	s_load_dwordx4 s[80:83], s[0:1], 0x0
	s_load_dwordx8 s[72:79], s[0:1], 0x18
	s_cmpk_ge_u32 s2, 0x200
	s_cbranch_scc1 .Lk2_prio
	s_setprio 1
	s_cmpk_ge_u32 s2, 0x100
	s_cbranch_scc1 .Lk2_prio
	s_setprio 3
